# K-loop load-segment slimming on best: trip counter/pointer increments + exit compare hoisted above the trip's final barrier (back-edge rotation), per-DMA v_mov address copies removed (source VGPR used
# speedup vs baseline: 1.0101x; 1.0101x over previous
; template <class Epi, bool GATHER, bool EXPERT, bool FP8>
; DI void gemm_phase(LAS unsigned char* lds, const Gemm g, const StaticOrder& S, const Epi& E) {
;     ...
;         for (int t = 0; t < nt; t += 2) {
;             const bool last = (t == nt - 2);
;             const char* a1 = cA + (size_t)(t + 1) * kstep;
;             const char* a2 = last ? nA : cA + (size_t)(t + 2) * kstep; const char* b2 = last ? nB : cB + (size_t)(t + 2) * kstep;
;             const char* a3 = a2 + kstep; const char* b3 = b2 + kstep;
;             unsigned o00 = coffA[0][0], o01 = coffA[0][1], o10 = coffA[1][0], o11 = coffA[1][1];
;             if (GATHER && last && has_next) {
;                 o00 = sp[0] * (unsigned)(K * 2) + (unsigned)C0x2; o01 = sp[512] * (unsigned)(K * 2) + (unsigned)C1x2;
;                 o10 = sp[1024] * (unsigned)(K * 2) + (unsigned)C0x2; o11 = sp[1536] * (unsigned)(K * 2) + (unsigned)C1x2; }
;             PG8_TRIP(a1, a2, b2, a3, b3, o00, o01, o10, o11);
.LBB0_115:
	ds_read_b128 v[130:133], v231
	ds_read_b128 v[134:137], v231 offset:1024
	ds_read_b128 v[138:141], v231 offset:2048
	ds_read_b128 v[142:145], v231 offset:3072
	ds_read_b128 v[146:149], v232
	ds_read_b128 v[150:153], v232 offset:1024
	ds_read_b128 v[154:157], v232 offset:2048
	ds_read_b128 v[158:161], v232 offset:3072
	s_add_u32 s0, s6, 0x80
	s_addc_u32 s1, s7, 0
	s_cmp_eq_u32 s18, 28
	s_cselect_b32 s9, s43, s1
	s_cselect_b32 s8, s42, s0
	s_cselect_b32 s1, s45, s15
	s_cselect_b32 s0, s44, s5
	ds_read_b128 v[162:165], v233
	ds_read_b128 v[166:169], v233 offset:1024
	ds_read_b128 v[170:173], v233 offset:2048
	ds_read_b128 v[174:177], v233 offset:3072
	ds_read_b128 v[178:181], v233 offset:4096
	ds_read_b128 v[182:185], v233 offset:5120
	ds_read_b128 v[192:195], v233 offset:6144
	ds_read_b128 v[196:199], v233 offset:7168
	s_add_i32 m0, s37, 0xc000
	s_nop 0
	global_load_lds_dwordx4 v227, s[6:7]
	s_add_i32 m0, s37, 0xe000
	s_nop 0
	global_load_lds_dwordx4 v229, s[6:7]
	s_waitcnt vmcnt(8)
	s_waitcnt lgkmcnt(0)
	s_barrier
	s_setprio 1
	s_waitcnt lgkmcnt(0)
	v_mfma_f32_16x16x32_bf16 v[126:129], v[130:133], v[162:165], v[126:129]
	v_mfma_f32_16x16x32_bf16 v[122:125], v[138:141], v[162:165], v[122:125]
	v_mfma_f32_16x16x32_bf16 v[118:121], v[130:133], v[170:173], v[118:121]
	v_mfma_f32_16x16x32_bf16 v[110:113], v[138:141], v[170:173], v[110:113]
	v_mfma_f32_16x16x32_bf16 v[102:105], v[130:133], v[178:181], v[102:105]
	v_mfma_f32_16x16x32_bf16 v[94:97], v[138:141], v[178:181], v[94:97]
	v_mfma_f32_16x16x32_bf16 v[86:89], v[130:133], v[192:195], v[86:89]
	v_mfma_f32_16x16x32_bf16 v[78:81], v[138:141], v[192:195], v[78:81]
	v_mfma_f32_16x16x32_bf16 v[126:129], v[134:137], v[166:169], v[126:129]
	v_mfma_f32_16x16x32_bf16 v[122:125], v[142:145], v[166:169], v[122:125]
	v_mfma_f32_16x16x32_bf16 v[118:121], v[134:137], v[174:177], v[118:121]
	v_mfma_f32_16x16x32_bf16 v[110:113], v[142:145], v[174:177], v[110:113]
	v_mfma_f32_16x16x32_bf16 v[102:105], v[134:137], v[182:185], v[102:105]
	v_mfma_f32_16x16x32_bf16 v[94:97], v[142:145], v[182:185], v[94:97]
	v_mfma_f32_16x16x32_bf16 v[86:89], v[134:137], v[196:199], v[86:89]
	v_mfma_f32_16x16x32_bf16 v[78:81], v[142:145], v[196:199], v[78:81]
	s_setprio 0
	s_setprio 1
	v_mfma_f32_16x16x32_bf16 v[114:117], v[146:149], v[162:165], v[114:117]
	v_mfma_f32_16x16x32_bf16 v[106:109], v[154:157], v[162:165], v[106:109]
	v_mfma_f32_16x16x32_bf16 v[98:101], v[146:149], v[170:173], v[98:101]
	v_mfma_f32_16x16x32_bf16 v[90:93], v[154:157], v[170:173], v[90:93]
	v_mfma_f32_16x16x32_bf16 v[82:85], v[146:149], v[178:181], v[82:85]
	v_mfma_f32_16x16x32_bf16 v[74:77], v[154:157], v[178:181], v[74:77]
	v_mfma_f32_16x16x32_bf16 v[70:73], v[146:149], v[192:195], v[70:73]
	v_mfma_f32_16x16x32_bf16 v[66:69], v[154:157], v[192:195], v[66:69]
	v_mfma_f32_16x16x32_bf16 v[114:117], v[150:153], v[166:169], v[114:117]
	v_mfma_f32_16x16x32_bf16 v[106:109], v[158:161], v[166:169], v[106:109]
	v_mfma_f32_16x16x32_bf16 v[98:101], v[150:153], v[174:177], v[98:101]
	v_mfma_f32_16x16x32_bf16 v[90:93], v[158:161], v[174:177], v[90:93]
	v_mfma_f32_16x16x32_bf16 v[82:85], v[150:153], v[182:185], v[82:85]
	v_mfma_f32_16x16x32_bf16 v[74:77], v[158:161], v[182:185], v[74:77]
	v_mfma_f32_16x16x32_bf16 v[70:73], v[150:153], v[196:199], v[70:73]
	v_mfma_f32_16x16x32_bf16 v[66:69], v[158:161], v[196:199], v[66:69]
	s_setprio 0
	s_barrier
	s_add_i32 s33, s75, s53
	ds_read_b128 v[162:165], v233 offset:16384
	ds_read_b128 v[166:169], v233 offset:17408
	ds_read_b128 v[170:173], v233 offset:18432
	ds_read_b128 v[174:177], v233 offset:19456
	ds_read_b128 v[178:181], v233 offset:20480
	ds_read_b128 v[182:185], v233 offset:21504
	ds_read_b128 v[192:195], v233 offset:22528
	ds_read_b128 v[196:199], v233 offset:23552
	s_mov_b32 m0, s33
	s_nop 0
	global_load_lds_dwordx4 v1, s[0:1]
	s_add_i32 m0, s33, 0x2000
	s_add_u32 s46, s0, 0x80000
	global_load_lds_dwordx4 v225, s[0:1]
	s_addc_u32 s47, s1, 0
	s_add_i32 s33, s76, s53
	s_mov_b32 m0, s33
	s_nop 0
	global_load_lds_dwordx4 v1, s[46:47]
	s_add_i32 m0, s33, 0x2000
	s_nop 0
	global_load_lds_dwordx4 v225, s[46:47]
	s_mov_b32 m0, s37
	s_nop 0
	global_load_lds_dwordx4 v226, s[8:9]
	s_mov_b32 m0, s54
	s_nop 0
	global_load_lds_dwordx4 v228, s[8:9]
	s_waitcnt vmcnt(8)
	s_waitcnt lgkmcnt(0)
	s_barrier
	s_setprio 1
	s_waitcnt lgkmcnt(0)
	v_mfma_f32_16x16x32_bf16 v[62:65], v[130:133], v[162:165], v[62:65]
	v_mfma_f32_16x16x32_bf16 v[58:61], v[138:141], v[162:165], v[58:61]
	v_mfma_f32_16x16x32_bf16 v[54:57], v[130:133], v[170:173], v[54:57]
	v_mfma_f32_16x16x32_bf16 v[46:49], v[138:141], v[170:173], v[46:49]
	v_mfma_f32_16x16x32_bf16 v[38:41], v[130:133], v[178:181], v[38:41]
	v_mfma_f32_16x16x32_bf16 v[30:33], v[138:141], v[178:181], v[30:33]
	v_mfma_f32_16x16x32_bf16 v[22:25], v[130:133], v[192:195], v[22:25]
	v_mfma_f32_16x16x32_bf16 v[14:17], v[138:141], v[192:195], v[14:17]
	v_mfma_f32_16x16x32_bf16 v[62:65], v[134:137], v[166:169], v[62:65]
	v_mfma_f32_16x16x32_bf16 v[58:61], v[142:145], v[166:169], v[58:61]
	v_mfma_f32_16x16x32_bf16 v[54:57], v[134:137], v[174:177], v[54:57]
	v_mfma_f32_16x16x32_bf16 v[46:49], v[142:145], v[174:177], v[46:49]
	v_mfma_f32_16x16x32_bf16 v[38:41], v[134:137], v[182:185], v[38:41]
	v_mfma_f32_16x16x32_bf16 v[30:33], v[142:145], v[182:185], v[30:33]
	v_mfma_f32_16x16x32_bf16 v[22:25], v[134:137], v[196:199], v[22:25]
	v_mfma_f32_16x16x32_bf16 v[14:17], v[142:145], v[196:199], v[14:17]
	s_setprio 0
	s_setprio 1
	v_mfma_f32_16x16x32_bf16 v[50:53], v[146:149], v[162:165], v[50:53]
	v_mfma_f32_16x16x32_bf16 v[42:45], v[154:157], v[162:165], v[42:45]
	v_mfma_f32_16x16x32_bf16 v[34:37], v[146:149], v[170:173], v[34:37]
	v_mfma_f32_16x16x32_bf16 v[26:29], v[154:157], v[170:173], v[26:29]
	v_mfma_f32_16x16x32_bf16 v[18:21], v[146:149], v[178:181], v[18:21]
	v_mfma_f32_16x16x32_bf16 v[10:13], v[154:157], v[178:181], v[10:13]
	v_mfma_f32_16x16x32_bf16 v[6:9], v[146:149], v[192:195], v[6:9]
	v_mfma_f32_16x16x32_bf16 v[2:5], v[154:157], v[192:195], v[2:5]
	v_mfma_f32_16x16x32_bf16 v[50:53], v[150:153], v[166:169], v[50:53]
	v_mfma_f32_16x16x32_bf16 v[42:45], v[158:161], v[166:169], v[42:45]
	v_mfma_f32_16x16x32_bf16 v[34:37], v[150:153], v[174:177], v[34:37]
	v_mfma_f32_16x16x32_bf16 v[26:29], v[158:161], v[174:177], v[26:29]
	v_mfma_f32_16x16x32_bf16 v[18:21], v[150:153], v[182:185], v[18:21]
	v_mfma_f32_16x16x32_bf16 v[10:13], v[158:161], v[182:185], v[10:13]
	v_mfma_f32_16x16x32_bf16 v[6:9], v[150:153], v[196:199], v[6:9]
	v_mfma_f32_16x16x32_bf16 v[2:5], v[158:161], v[196:199], v[2:5]
	s_setprio 0
	s_barrier
	s_add_i32 s33, 0, 0x18000
	s_add_i32 s39, 0, 0x1c000
	v_add_u32_e32 v142, s33, v230
	v_add_u32_e32 v158, s39, v230
	ds_read_b128 v[130:133], v142
	ds_read_b128 v[134:137], v142 offset:1024
	ds_read_b128 v[138:141], v142 offset:2048
	ds_read_b128 v[142:145], v142 offset:3072
	ds_read_b128 v[146:149], v158
	ds_read_b128 v[150:153], v158 offset:1024
	ds_read_b128 v[154:157], v158 offset:2048
	ds_read_b128 v[158:161], v158 offset:3072
	s_mov_b32 m0, s55
	ds_read_b128 v[162:165], v233 offset:32768
	ds_read_b128 v[166:169], v233 offset:33792
	ds_read_b128 v[170:173], v233 offset:34816
	ds_read_b128 v[174:177], v233 offset:35840
	ds_read_b128 v[178:181], v233 offset:36864
	ds_read_b128 v[182:185], v233 offset:37888
	ds_read_b128 v[192:195], v233 offset:38912
	ds_read_b128 v[196:199], v233 offset:39936
	s_nop 0
	global_load_lds_dwordx4 v227, s[8:9]
	s_mov_b32 m0, s56
	s_nop 0
	global_load_lds_dwordx4 v229, s[8:9]
	s_waitcnt vmcnt(8)
	s_waitcnt lgkmcnt(0)
	s_barrier
	s_setprio 1
	s_waitcnt lgkmcnt(0)
	v_mfma_f32_16x16x32_bf16 v[126:129], v[130:133], v[162:165], v[126:129]
	v_mfma_f32_16x16x32_bf16 v[122:125], v[138:141], v[162:165], v[122:125]
	v_mfma_f32_16x16x32_bf16 v[118:121], v[130:133], v[170:173], v[118:121]
	v_mfma_f32_16x16x32_bf16 v[110:113], v[138:141], v[170:173], v[110:113]
	v_mfma_f32_16x16x32_bf16 v[102:105], v[130:133], v[178:181], v[102:105]
	v_mfma_f32_16x16x32_bf16 v[94:97], v[138:141], v[178:181], v[94:97]
	v_mfma_f32_16x16x32_bf16 v[86:89], v[130:133], v[192:195], v[86:89]
	v_mfma_f32_16x16x32_bf16 v[78:81], v[138:141], v[192:195], v[78:81]
	v_mfma_f32_16x16x32_bf16 v[126:129], v[134:137], v[166:169], v[126:129]
	v_mfma_f32_16x16x32_bf16 v[122:125], v[142:145], v[166:169], v[122:125]
	v_mfma_f32_16x16x32_bf16 v[118:121], v[134:137], v[174:177], v[118:121]
	v_mfma_f32_16x16x32_bf16 v[110:113], v[142:145], v[174:177], v[110:113]
	v_mfma_f32_16x16x32_bf16 v[102:105], v[134:137], v[182:185], v[102:105]
	v_mfma_f32_16x16x32_bf16 v[94:97], v[142:145], v[182:185], v[94:97]
	v_mfma_f32_16x16x32_bf16 v[86:89], v[134:137], v[196:199], v[86:89]
	v_mfma_f32_16x16x32_bf16 v[78:81], v[142:145], v[196:199], v[78:81]
	s_setprio 0
	s_setprio 1
	v_mfma_f32_16x16x32_bf16 v[114:117], v[146:149], v[162:165], v[114:117]
	v_mfma_f32_16x16x32_bf16 v[106:109], v[154:157], v[162:165], v[106:109]
	v_mfma_f32_16x16x32_bf16 v[98:101], v[146:149], v[170:173], v[98:101]
	v_mfma_f32_16x16x32_bf16 v[90:93], v[154:157], v[170:173], v[90:93]
	v_mfma_f32_16x16x32_bf16 v[82:85], v[146:149], v[178:181], v[82:85]
	v_mfma_f32_16x16x32_bf16 v[74:77], v[154:157], v[178:181], v[74:77]
	v_mfma_f32_16x16x32_bf16 v[70:73], v[146:149], v[192:195], v[70:73]
	v_mfma_f32_16x16x32_bf16 v[66:69], v[154:157], v[192:195], v[66:69]
	v_mfma_f32_16x16x32_bf16 v[114:117], v[150:153], v[166:169], v[114:117]
	v_mfma_f32_16x16x32_bf16 v[106:109], v[158:161], v[166:169], v[106:109]
	v_mfma_f32_16x16x32_bf16 v[98:101], v[150:153], v[174:177], v[98:101]
	v_mfma_f32_16x16x32_bf16 v[90:93], v[158:161], v[174:177], v[90:93]
	v_mfma_f32_16x16x32_bf16 v[82:85], v[150:153], v[182:185], v[82:85]
	v_mfma_f32_16x16x32_bf16 v[74:77], v[158:161], v[182:185], v[74:77]
	v_mfma_f32_16x16x32_bf16 v[70:73], v[150:153], v[196:199], v[70:73]
	v_mfma_f32_16x16x32_bf16 v[66:69], v[158:161], v[196:199], v[66:69]
	s_setprio 0
	s_barrier
; template <class Epi, bool GATHER, bool EXPERT, bool FP8>
; DI void gemm_phase(LAS unsigned char* lds, const Gemm g, const StaticOrder& S, const Epi& E) {
;     ...
;         for (int t = 0; t < nt; t += 2) {
;             const bool last = (t == nt - 2);
;             const char* a1 = cA + (size_t)(t + 1) * kstep;
;             const char* a2 = last ? nA : cA + (size_t)(t + 2) * kstep; const char* b2 = last ? nB : cB + (size_t)(t + 2) * kstep;
;             const char* a3 = a2 + kstep; const char* b3 = b2 + kstep;
;             unsigned o00 = coffA[0][0], o01 = coffA[0][1], o10 = coffA[1][0], o11 = coffA[1][1];
;             if (GATHER && last && has_next) {
;                 o00 = sp[0] * (unsigned)(K * 2) + (unsigned)C0x2; o01 = sp[512] * (unsigned)(K * 2) + (unsigned)C1x2;
;                 o10 = sp[1024] * (unsigned)(K * 2) + (unsigned)C0x2; o11 = sp[1536] * (unsigned)(K * 2) + (unsigned)C1x2; }
;             PG8_TRIP(a1, a2, b2, a3, b3, o00, o01, o10, o11);
;             if (last) { coffA[0][0] = o00; coffA[0][1] = o01; coffA[1][0] = o10; coffA[1][1] = o11; }
;         }
	v_mov_b32_e32 v186, v1
	ds_read_b128 v[162:165], v233 offset:49152
	ds_read_b128 v[166:169], v233 offset:50176
	ds_read_b128 v[170:173], v233 offset:51200
	ds_read_b128 v[174:177], v233 offset:52224
	ds_read_b128 v[178:181], v233 offset:53248
	ds_read_b128 v[182:185], v233 offset:54272
	ds_read_b128 v[192:195], v233 offset:55296
	ds_read_b128 v[196:199], v233 offset:56320
	s_add_i32 s33, s33, s53
	v_lshl_add_u64 v[200:201], s[0:1], 0, v[186:187]
	v_lshl_add_u64 v[200:201], v[200:201], 0, s[24:25]
	s_mov_b32 m0, s33
	v_mov_b32_e32 v186, v225
	global_load_lds_dwordx4 v[200:201], off
	s_add_i32 m0, s33, 0x2000
	s_nop 0
	v_lshl_add_u64 v[200:201], s[0:1], 0, v[186:187]
	s_add_u32 s0, s0, 0x80080
	v_lshl_add_u64 v[200:201], v[200:201], 0, s[24:25]
	s_addc_u32 s1, s1, 0
	s_add_i32 s33, s39, s53
	global_load_lds_dwordx4 v[200:201], off
	s_mov_b32 m0, s33
	s_nop 0
	global_load_lds_dwordx4 v1, s[0:1]
	s_add_i32 m0, s33, 0x2000
	s_nop 0
	global_load_lds_dwordx4 v225, s[0:1]
	v_mov_b32_e32 v186, v226
	s_mov_b32 m0, s62
	v_lshl_add_u64 v[200:201], s[8:9], 0, v[186:187]
	v_lshl_add_u64 v[200:201], v[200:201], 0, s[24:25]
	v_mov_b32_e32 v186, v228
	global_load_lds_dwordx4 v[200:201], off
	s_mov_b32 m0, s63
	v_lshl_add_u64 v[200:201], s[8:9], 0, v[186:187]
	v_lshl_add_u64 v[200:201], v[200:201], 0, s[24:25]
	global_load_lds_dwordx4 v[200:201], off
	s_waitcnt vmcnt(8)
	s_waitcnt lgkmcnt(0)
	s_barrier
	s_setprio 1
	s_waitcnt lgkmcnt(0)
	v_mfma_f32_16x16x32_bf16 v[62:65], v[130:133], v[162:165], v[62:65]
	v_mfma_f32_16x16x32_bf16 v[58:61], v[138:141], v[162:165], v[58:61]
	v_mfma_f32_16x16x32_bf16 v[54:57], v[130:133], v[170:173], v[54:57]
	v_mfma_f32_16x16x32_bf16 v[46:49], v[138:141], v[170:173], v[46:49]
	v_mfma_f32_16x16x32_bf16 v[38:41], v[130:133], v[178:181], v[38:41]
	v_mfma_f32_16x16x32_bf16 v[30:33], v[138:141], v[178:181], v[30:33]
	v_mfma_f32_16x16x32_bf16 v[22:25], v[130:133], v[192:195], v[22:25]
	v_mfma_f32_16x16x32_bf16 v[14:17], v[138:141], v[192:195], v[14:17]
	v_mfma_f32_16x16x32_bf16 v[62:65], v[134:137], v[166:169], v[62:65]
	v_mfma_f32_16x16x32_bf16 v[58:61], v[142:145], v[166:169], v[58:61]
	v_mfma_f32_16x16x32_bf16 v[54:57], v[134:137], v[174:177], v[54:57]
	v_mfma_f32_16x16x32_bf16 v[46:49], v[142:145], v[174:177], v[46:49]
	v_mfma_f32_16x16x32_bf16 v[38:41], v[134:137], v[182:185], v[38:41]
	v_mfma_f32_16x16x32_bf16 v[30:33], v[142:145], v[182:185], v[30:33]
	v_mfma_f32_16x16x32_bf16 v[22:25], v[134:137], v[196:199], v[22:25]
	v_mfma_f32_16x16x32_bf16 v[14:17], v[142:145], v[196:199], v[14:17]
	s_setprio 0
	s_setprio 1
	v_mfma_f32_16x16x32_bf16 v[50:53], v[146:149], v[162:165], v[50:53]
	v_mfma_f32_16x16x32_bf16 v[42:45], v[154:157], v[162:165], v[42:45]
	v_mfma_f32_16x16x32_bf16 v[34:37], v[146:149], v[170:173], v[34:37]
	v_mfma_f32_16x16x32_bf16 v[26:29], v[154:157], v[170:173], v[26:29]
	v_mfma_f32_16x16x32_bf16 v[18:21], v[146:149], v[178:181], v[18:21]
	v_mfma_f32_16x16x32_bf16 v[10:13], v[154:157], v[178:181], v[10:13]
	v_mfma_f32_16x16x32_bf16 v[6:9], v[146:149], v[192:195], v[6:9]
	v_mfma_f32_16x16x32_bf16 v[2:5], v[154:157], v[192:195], v[2:5]
	v_mfma_f32_16x16x32_bf16 v[50:53], v[150:153], v[166:169], v[50:53]
	v_mfma_f32_16x16x32_bf16 v[42:45], v[158:161], v[166:169], v[42:45]
	v_mfma_f32_16x16x32_bf16 v[34:37], v[150:153], v[174:177], v[34:37]
	v_mfma_f32_16x16x32_bf16 v[26:29], v[158:161], v[174:177], v[26:29]
	v_mfma_f32_16x16x32_bf16 v[18:21], v[150:153], v[182:185], v[18:21]
	v_mfma_f32_16x16x32_bf16 v[10:13], v[158:161], v[182:185], v[10:13]
	v_mfma_f32_16x16x32_bf16 v[6:9], v[150:153], v[196:199], v[6:9]
	v_mfma_f32_16x16x32_bf16 v[2:5], v[158:161], v[196:199], v[2:5]
	s_add_i32 s18, s18, 2
	s_add_u32 s5, s5, 0x100
	s_addc_u32 s15, s15, 0
	s_add_u32 s6, s6, 0x100
	s_addc_u32 s7, s7, 0
	s_cmp_gt_u32 s18, 29
	s_setprio 0
	s_barrier
	s_cbranch_scc0 .LBB0_115
	s_and_b64 vcc, exec, s[26:27]
	s_cbranch_vccz .LBB0_118
	s_barrier

.LBB0_793:
	ds_read_b128 v[136:139], v148
	ds_read_b128 v[152:155], v148 offset:1024
	ds_read_b128 v[156:159], v148 offset:2048
	ds_read_b128 v[160:163], v148 offset:3072
	ds_read_b128 v[164:167], v149
	ds_read_b128 v[168:171], v149 offset:1024
	ds_read_b128 v[172:175], v149 offset:2048
	ds_read_b128 v[176:179], v149 offset:3072
	s_add_u32 s0, s30, 0x80
	s_addc_u32 s1, s31, 0
	s_cmp_eq_u32 s55, 28
	s_cselect_b32 s35, s25, s1
	s_cselect_b32 s34, s24, s0
	s_cselect_b32 s1, s27, s23
	s_cselect_b32 s0, s26, s21
	ds_read_b128 v[180:183], v150
	ds_read_b128 v[184:187], v150 offset:1024
	ds_read_b128 v[188:191], v150 offset:2048
	ds_read_b128 v[192:195], v150 offset:3072
	ds_read_b128 v[196:199], v150 offset:4096
	ds_read_b128 v[200:203], v150 offset:5120
	ds_read_b128 v[204:207], v150 offset:6144
	ds_read_b128 v[208:211], v150 offset:7168
	s_add_i32 m0, s29, 0xc000
	s_nop 0
	global_load_lds_dwordx4 v144, s[30:31]
	s_add_i32 m0, s29, 0xe000
	s_nop 0
	global_load_lds_dwordx4 v146, s[30:31]
	s_waitcnt vmcnt(8)
	s_waitcnt lgkmcnt(0)
	s_barrier
	s_setprio 1
	s_waitcnt lgkmcnt(0)
	v_mfma_f32_16x16x32_bf16 v[126:129], v[136:139], v[180:183], v[126:129]
	v_mfma_f32_16x16x32_bf16 v[122:125], v[156:159], v[180:183], v[122:125]
	v_mfma_f32_16x16x32_bf16 v[118:121], v[136:139], v[188:191], v[118:121]
	v_mfma_f32_16x16x32_bf16 v[114:117], v[156:159], v[188:191], v[114:117]
	v_mfma_f32_16x16x32_bf16 v[110:113], v[136:139], v[196:199], v[110:113]
	v_mfma_f32_16x16x32_bf16 v[90:93], v[156:159], v[196:199], v[90:93]
	v_mfma_f32_16x16x32_bf16 v[82:85], v[136:139], v[204:207], v[82:85]
	v_mfma_f32_16x16x32_bf16 v[74:77], v[156:159], v[204:207], v[74:77]
	v_mfma_f32_16x16x32_bf16 v[126:129], v[152:155], v[184:187], v[126:129]
	v_mfma_f32_16x16x32_bf16 v[122:125], v[160:163], v[184:187], v[122:125]
	v_mfma_f32_16x16x32_bf16 v[118:121], v[152:155], v[192:195], v[118:121]
	v_mfma_f32_16x16x32_bf16 v[114:117], v[160:163], v[192:195], v[114:117]
	v_mfma_f32_16x16x32_bf16 v[110:113], v[152:155], v[200:203], v[110:113]
	v_mfma_f32_16x16x32_bf16 v[90:93], v[160:163], v[200:203], v[90:93]
	v_mfma_f32_16x16x32_bf16 v[82:85], v[152:155], v[208:211], v[82:85]
	v_mfma_f32_16x16x32_bf16 v[74:77], v[160:163], v[208:211], v[74:77]
	s_setprio 0
	s_setprio 1
	v_mfma_f32_16x16x32_bf16 v[106:109], v[164:167], v[180:183], v[106:109]
	v_mfma_f32_16x16x32_bf16 v[102:105], v[172:175], v[180:183], v[102:105]
	v_mfma_f32_16x16x32_bf16 v[98:101], v[164:167], v[188:191], v[98:101]
	v_mfma_f32_16x16x32_bf16 v[94:97], v[172:175], v[188:191], v[94:97]
	v_mfma_f32_16x16x32_bf16 v[86:89], v[164:167], v[196:199], v[86:89]
	v_mfma_f32_16x16x32_bf16 v[78:81], v[172:175], v[196:199], v[78:81]
	v_mfma_f32_16x16x32_bf16 v[70:73], v[164:167], v[204:207], v[70:73]
	v_mfma_f32_16x16x32_bf16 v[66:69], v[172:175], v[204:207], v[66:69]
	v_mfma_f32_16x16x32_bf16 v[106:109], v[168:171], v[184:187], v[106:109]
	v_mfma_f32_16x16x32_bf16 v[102:105], v[176:179], v[184:187], v[102:105]
	v_mfma_f32_16x16x32_bf16 v[98:101], v[168:171], v[192:195], v[98:101]
	v_mfma_f32_16x16x32_bf16 v[94:97], v[176:179], v[192:195], v[94:97]
	v_mfma_f32_16x16x32_bf16 v[86:89], v[168:171], v[200:203], v[86:89]
	v_mfma_f32_16x16x32_bf16 v[78:81], v[176:179], v[200:203], v[78:81]
	v_mfma_f32_16x16x32_bf16 v[70:73], v[168:171], v[208:211], v[70:73]
	v_mfma_f32_16x16x32_bf16 v[66:69], v[176:179], v[208:211], v[66:69]
	s_setprio 0
	s_barrier
	s_add_i32 s56, s50, s40
	ds_read_b128 v[180:183], v150 offset:16384
	ds_read_b128 v[184:187], v150 offset:17408
	ds_read_b128 v[188:191], v150 offset:18432
	ds_read_b128 v[192:195], v150 offset:19456
	ds_read_b128 v[196:199], v150 offset:20480
	ds_read_b128 v[200:203], v150 offset:21504
	ds_read_b128 v[204:207], v150 offset:22528
	ds_read_b128 v[208:211], v150 offset:23552
	s_mov_b32 m0, s56
	s_nop 0
	global_load_lds_dwordx4 v1, s[0:1]
	s_add_i32 m0, s56, 0x2000
	s_add_u32 s56, s0, 0x80000
	global_load_lds_dwordx4 v142, s[0:1]
	s_addc_u32 s57, s1, 0
	s_add_i32 s58, s51, s40
	s_mov_b32 m0, s58
	s_nop 0
	global_load_lds_dwordx4 v1, s[56:57]
	s_add_i32 m0, s58, 0x2000
	s_nop 0
	global_load_lds_dwordx4 v142, s[56:57]
	s_mov_b32 m0, s29
	s_nop 0
	global_load_lds_dwordx4 v143, s[34:35]
	s_mov_b32 m0, s41
	s_nop 0
	global_load_lds_dwordx4 v145, s[34:35]
	s_waitcnt vmcnt(8)
	s_waitcnt lgkmcnt(0)
	s_barrier
	s_setprio 1
	s_waitcnt lgkmcnt(0)
	v_mfma_f32_16x16x32_bf16 v[62:65], v[136:139], v[180:183], v[62:65]
	v_mfma_f32_16x16x32_bf16 v[58:61], v[156:159], v[180:183], v[58:61]
	v_mfma_f32_16x16x32_bf16 v[54:57], v[136:139], v[188:191], v[54:57]
	v_mfma_f32_16x16x32_bf16 v[50:53], v[156:159], v[188:191], v[50:53]
	v_mfma_f32_16x16x32_bf16 v[42:45], v[136:139], v[196:199], v[42:45]
	v_mfma_f32_16x16x32_bf16 v[34:37], v[156:159], v[196:199], v[34:37]
	v_mfma_f32_16x16x32_bf16 v[22:25], v[136:139], v[204:207], v[22:25]
	v_mfma_f32_16x16x32_bf16 v[10:13], v[156:159], v[204:207], v[10:13]
	v_mfma_f32_16x16x32_bf16 v[62:65], v[152:155], v[184:187], v[62:65]
	v_mfma_f32_16x16x32_bf16 v[58:61], v[160:163], v[184:187], v[58:61]
	v_mfma_f32_16x16x32_bf16 v[54:57], v[152:155], v[192:195], v[54:57]
	v_mfma_f32_16x16x32_bf16 v[50:53], v[160:163], v[192:195], v[50:53]
	v_mfma_f32_16x16x32_bf16 v[42:45], v[152:155], v[200:203], v[42:45]
	v_mfma_f32_16x16x32_bf16 v[34:37], v[160:163], v[200:203], v[34:37]
	v_mfma_f32_16x16x32_bf16 v[22:25], v[152:155], v[208:211], v[22:25]
	v_mfma_f32_16x16x32_bf16 v[10:13], v[160:163], v[208:211], v[10:13]
	s_setprio 0
	s_setprio 1
	v_mfma_f32_16x16x32_bf16 v[46:49], v[164:167], v[180:183], v[46:49]
	v_mfma_f32_16x16x32_bf16 v[38:41], v[172:175], v[180:183], v[38:41]
	v_mfma_f32_16x16x32_bf16 v[30:33], v[164:167], v[188:191], v[30:33]
	v_mfma_f32_16x16x32_bf16 v[26:29], v[172:175], v[188:191], v[26:29]
	v_mfma_f32_16x16x32_bf16 v[18:21], v[164:167], v[196:199], v[18:21]
	v_mfma_f32_16x16x32_bf16 v[14:17], v[172:175], v[196:199], v[14:17]
	v_mfma_f32_16x16x32_bf16 v[6:9], v[164:167], v[204:207], v[6:9]
	v_mfma_f32_16x16x32_bf16 v[2:5], v[172:175], v[204:207], v[2:5]
	v_mfma_f32_16x16x32_bf16 v[46:49], v[168:171], v[184:187], v[46:49]
	v_mfma_f32_16x16x32_bf16 v[38:41], v[176:179], v[184:187], v[38:41]
	v_mfma_f32_16x16x32_bf16 v[30:33], v[168:171], v[192:195], v[30:33]
	v_mfma_f32_16x16x32_bf16 v[26:29], v[176:179], v[192:195], v[26:29]
	v_mfma_f32_16x16x32_bf16 v[18:21], v[168:171], v[200:203], v[18:21]
	v_mfma_f32_16x16x32_bf16 v[14:17], v[176:179], v[200:203], v[14:17]
	v_mfma_f32_16x16x32_bf16 v[6:9], v[168:171], v[208:211], v[6:9]
	v_mfma_f32_16x16x32_bf16 v[2:5], v[176:179], v[208:211], v[2:5]
	s_setprio 0
	s_barrier
	s_add_i32 s56, 0, 0x18000
	v_add_u32_e32 v130, s56, v147
	s_add_i32 s57, 0, 0x1c000
	ds_read_b128 v[136:139], v130
	ds_read_b128 v[152:155], v130 offset:1024
	ds_read_b128 v[156:159], v130 offset:2048
	ds_read_b128 v[160:163], v130 offset:3072
	v_add_u32_e32 v130, s57, v147
	ds_read_b128 v[164:167], v130
	ds_read_b128 v[168:171], v130 offset:1024
	ds_read_b128 v[172:175], v130 offset:2048
	ds_read_b128 v[176:179], v130 offset:3072
	s_mov_b32 m0, s42
	ds_read_b128 v[180:183], v150 offset:32768
	ds_read_b128 v[184:187], v150 offset:33792
	ds_read_b128 v[188:191], v150 offset:34816
	ds_read_b128 v[192:195], v150 offset:35840
	ds_read_b128 v[196:199], v150 offset:36864
	ds_read_b128 v[200:203], v150 offset:37888
	ds_read_b128 v[204:207], v150 offset:38912
	ds_read_b128 v[208:211], v150 offset:39936
	s_nop 0
	global_load_lds_dwordx4 v144, s[34:35]
	s_mov_b32 m0, s43
	s_nop 0
	global_load_lds_dwordx4 v146, s[34:35]
	s_waitcnt vmcnt(8)
	s_waitcnt lgkmcnt(0)
	s_barrier
	s_setprio 1
	s_waitcnt lgkmcnt(0)
	v_mfma_f32_16x16x32_bf16 v[126:129], v[136:139], v[180:183], v[126:129]
	v_mfma_f32_16x16x32_bf16 v[122:125], v[156:159], v[180:183], v[122:125]
	v_mfma_f32_16x16x32_bf16 v[118:121], v[136:139], v[188:191], v[118:121]
	v_mfma_f32_16x16x32_bf16 v[114:117], v[156:159], v[188:191], v[114:117]
	v_mfma_f32_16x16x32_bf16 v[110:113], v[136:139], v[196:199], v[110:113]
	v_mfma_f32_16x16x32_bf16 v[90:93], v[156:159], v[196:199], v[90:93]
	v_mfma_f32_16x16x32_bf16 v[82:85], v[136:139], v[204:207], v[82:85]
	v_mfma_f32_16x16x32_bf16 v[74:77], v[156:159], v[204:207], v[74:77]
	v_mfma_f32_16x16x32_bf16 v[126:129], v[152:155], v[184:187], v[126:129]
	v_mfma_f32_16x16x32_bf16 v[122:125], v[160:163], v[184:187], v[122:125]
	v_mfma_f32_16x16x32_bf16 v[118:121], v[152:155], v[192:195], v[118:121]
	v_mfma_f32_16x16x32_bf16 v[114:117], v[160:163], v[192:195], v[114:117]
	v_mfma_f32_16x16x32_bf16 v[110:113], v[152:155], v[200:203], v[110:113]
	v_mfma_f32_16x16x32_bf16 v[90:93], v[160:163], v[200:203], v[90:93]
	v_mfma_f32_16x16x32_bf16 v[82:85], v[152:155], v[208:211], v[82:85]
	v_mfma_f32_16x16x32_bf16 v[74:77], v[160:163], v[208:211], v[74:77]
	s_setprio 0
	s_setprio 1
	v_mfma_f32_16x16x32_bf16 v[106:109], v[164:167], v[180:183], v[106:109]
	v_mfma_f32_16x16x32_bf16 v[102:105], v[172:175], v[180:183], v[102:105]
	v_mfma_f32_16x16x32_bf16 v[98:101], v[164:167], v[188:191], v[98:101]
	v_mfma_f32_16x16x32_bf16 v[94:97], v[172:175], v[188:191], v[94:97]
	v_mfma_f32_16x16x32_bf16 v[86:89], v[164:167], v[196:199], v[86:89]
	v_mfma_f32_16x16x32_bf16 v[78:81], v[172:175], v[196:199], v[78:81]
	v_mfma_f32_16x16x32_bf16 v[70:73], v[164:167], v[204:207], v[70:73]
	v_mfma_f32_16x16x32_bf16 v[66:69], v[172:175], v[204:207], v[66:69]
	v_mfma_f32_16x16x32_bf16 v[106:109], v[168:171], v[184:187], v[106:109]
	v_mfma_f32_16x16x32_bf16 v[102:105], v[176:179], v[184:187], v[102:105]
	v_mfma_f32_16x16x32_bf16 v[98:101], v[168:171], v[192:195], v[98:101]
	v_mfma_f32_16x16x32_bf16 v[94:97], v[176:179], v[192:195], v[94:97]
	v_mfma_f32_16x16x32_bf16 v[86:89], v[168:171], v[200:203], v[86:89]
	v_mfma_f32_16x16x32_bf16 v[78:81], v[176:179], v[200:203], v[78:81]
	v_mfma_f32_16x16x32_bf16 v[70:73], v[168:171], v[208:211], v[70:73]
	v_mfma_f32_16x16x32_bf16 v[66:69], v[176:179], v[208:211], v[66:69]
	s_setprio 0
	s_barrier
; template <class Epi, bool GATHER, bool EXPERT, bool FP8>
; DI void gemm_phase(LAS unsigned char* lds, const Gemm g, const StaticOrder& S, const Epi& E) {
;     ...
;         for (int t = 0; t < nt; t += 2) {
;             const bool last = (t == nt - 2);
;             const char* a1 = cA + (size_t)(t + 1) * kstep;
;             const char* a2 = last ? nA : cA + (size_t)(t + 2) * kstep; const char* b2 = last ? nB : cB + (size_t)(t + 2) * kstep;
;             const char* a3 = a2 + kstep; const char* b3 = b2 + kstep;
;             unsigned o00 = coffA[0][0], o01 = coffA[0][1], o10 = coffA[1][0], o11 = coffA[1][1];
;             if (GATHER && last && has_next) {
;                 o00 = sp[0] * (unsigned)(K * 2) + (unsigned)C0x2; o01 = sp[512] * (unsigned)(K * 2) + (unsigned)C1x2;
;                 o10 = sp[1024] * (unsigned)(K * 2) + (unsigned)C0x2; o11 = sp[1536] * (unsigned)(K * 2) + (unsigned)C1x2; }
;             PG8_TRIP(a1, a2, b2, a3, b3, o00, o01, o10, o11);
;             if (last) { coffA[0][0] = o00; coffA[0][1] = o01; coffA[1][0] = o10; coffA[1][1] = o11; }
;         }
	v_mov_b32_e32 v130, v1
	ds_read_b128 v[180:183], v150 offset:49152
	ds_read_b128 v[184:187], v150 offset:50176
	ds_read_b128 v[188:191], v150 offset:51200
	ds_read_b128 v[192:195], v150 offset:52224
	ds_read_b128 v[196:199], v150 offset:53248
	ds_read_b128 v[200:203], v150 offset:54272
	ds_read_b128 v[204:207], v150 offset:55296
	ds_read_b128 v[208:211], v150 offset:56320
	s_add_i32 s56, s56, s40
	v_lshl_add_u64 v[140:141], s[0:1], 0, v[130:131]
	v_lshl_add_u64 v[140:141], v[140:141], 0, s[68:69]
	s_mov_b32 m0, s56
	v_mov_b32_e32 v130, v142
	global_load_lds_dwordx4 v[140:141], off
	s_add_i32 m0, s56, 0x2000
	s_nop 0
	v_lshl_add_u64 v[140:141], s[0:1], 0, v[130:131]
	s_add_u32 s0, s0, 0x80080
	v_lshl_add_u64 v[140:141], v[140:141], 0, s[68:69]
	s_addc_u32 s1, s1, 0
	s_add_i32 s56, s57, s40
	global_load_lds_dwordx4 v[140:141], off
	s_mov_b32 m0, s56
	s_nop 0
	global_load_lds_dwordx4 v1, s[0:1]
	s_add_i32 m0, s56, 0x2000
	s_nop 0
	global_load_lds_dwordx4 v142, s[0:1]
	v_mov_b32_e32 v130, v143
	s_mov_b32 m0, s47
	v_lshl_add_u64 v[140:141], s[34:35], 0, v[130:131]
	v_lshl_add_u64 v[140:141], v[140:141], 0, s[68:69]
	v_mov_b32_e32 v130, v145
	global_load_lds_dwordx4 v[140:141], off
	s_mov_b32 m0, s48
	v_lshl_add_u64 v[140:141], s[34:35], 0, v[130:131]
	v_lshl_add_u64 v[140:141], v[140:141], 0, s[68:69]
	global_load_lds_dwordx4 v[140:141], off
	s_waitcnt vmcnt(8)
	s_waitcnt lgkmcnt(0)
	s_barrier
	s_setprio 1
	s_waitcnt lgkmcnt(0)
	v_mfma_f32_16x16x32_bf16 v[62:65], v[136:139], v[180:183], v[62:65]
	v_mfma_f32_16x16x32_bf16 v[58:61], v[156:159], v[180:183], v[58:61]
	v_mfma_f32_16x16x32_bf16 v[54:57], v[136:139], v[188:191], v[54:57]
	v_mfma_f32_16x16x32_bf16 v[50:53], v[156:159], v[188:191], v[50:53]
	v_mfma_f32_16x16x32_bf16 v[42:45], v[136:139], v[196:199], v[42:45]
	v_mfma_f32_16x16x32_bf16 v[34:37], v[156:159], v[196:199], v[34:37]
	v_mfma_f32_16x16x32_bf16 v[22:25], v[136:139], v[204:207], v[22:25]
	v_mfma_f32_16x16x32_bf16 v[10:13], v[156:159], v[204:207], v[10:13]
	v_mfma_f32_16x16x32_bf16 v[62:65], v[152:155], v[184:187], v[62:65]
	v_mfma_f32_16x16x32_bf16 v[58:61], v[160:163], v[184:187], v[58:61]
	v_mfma_f32_16x16x32_bf16 v[54:57], v[152:155], v[192:195], v[54:57]
	v_mfma_f32_16x16x32_bf16 v[50:53], v[160:163], v[192:195], v[50:53]
	v_mfma_f32_16x16x32_bf16 v[42:45], v[152:155], v[200:203], v[42:45]
	v_mfma_f32_16x16x32_bf16 v[34:37], v[160:163], v[200:203], v[34:37]
	v_mfma_f32_16x16x32_bf16 v[22:25], v[152:155], v[208:211], v[22:25]
	v_mfma_f32_16x16x32_bf16 v[10:13], v[160:163], v[208:211], v[10:13]
	s_setprio 0
	s_setprio 1
	v_mfma_f32_16x16x32_bf16 v[46:49], v[164:167], v[180:183], v[46:49]
	v_mfma_f32_16x16x32_bf16 v[38:41], v[172:175], v[180:183], v[38:41]
	v_mfma_f32_16x16x32_bf16 v[30:33], v[164:167], v[188:191], v[30:33]
	v_mfma_f32_16x16x32_bf16 v[26:29], v[172:175], v[188:191], v[26:29]
	v_mfma_f32_16x16x32_bf16 v[18:21], v[164:167], v[196:199], v[18:21]
	v_mfma_f32_16x16x32_bf16 v[14:17], v[172:175], v[196:199], v[14:17]
	v_mfma_f32_16x16x32_bf16 v[6:9], v[164:167], v[204:207], v[6:9]
	v_mfma_f32_16x16x32_bf16 v[2:5], v[172:175], v[204:207], v[2:5]
	v_mfma_f32_16x16x32_bf16 v[46:49], v[168:171], v[184:187], v[46:49]
	v_mfma_f32_16x16x32_bf16 v[38:41], v[176:179], v[184:187], v[38:41]
	v_mfma_f32_16x16x32_bf16 v[30:33], v[168:171], v[192:195], v[30:33]
	v_mfma_f32_16x16x32_bf16 v[26:29], v[176:179], v[192:195], v[26:29]
	v_mfma_f32_16x16x32_bf16 v[18:21], v[168:171], v[200:203], v[18:21]
	v_mfma_f32_16x16x32_bf16 v[14:17], v[176:179], v[200:203], v[14:17]
	v_mfma_f32_16x16x32_bf16 v[6:9], v[168:171], v[208:211], v[6:9]
	v_mfma_f32_16x16x32_bf16 v[2:5], v[176:179], v[208:211], v[2:5]
	s_add_i32 s55, s55, 2
	s_add_u32 s21, s21, 0x100
	s_addc_u32 s23, s23, 0
	s_add_u32 s30, s30, 0x100
	s_addc_u32 s31, s31, 0
	s_cmp_gt_u32 s55, 29
	s_setprio 0
	s_barrier
	s_cbranch_scc0 .LBB0_793
	s_and_b64 vcc, exec, s[72:73]
	s_cbranch_vccz .LBB0_796
	s_barrier

; template <class Epi, bool GATHER, bool EXPERT, bool FP8>
; DI void gemm_phase(LAS unsigned char* lds, const Gemm g, const StaticOrder& S, const Epi& E) {
;     ...
;         for (int t = 0; t < nt; t += 2) {
;             const bool last = (t == nt - 2);
.LBB0_1084:
	s_cmp_gt_u32 s0, 13
	s_cbranch_scc1 .LBB0_1089

.LBB0_1087:
	v_add_u32_e32 v110, s67, v164
	ds_read_b128 v[168:171], v110
	ds_read_b128 v[172:175], v110 offset:1024
	ds_read_b128 v[176:179], v110 offset:2048
	ds_read_b128 v[180:183], v110 offset:3072
	v_add_u32_e32 v110, s68, v164
	ds_read_b128 v[184:187], v110
	ds_read_b128 v[188:191], v110 offset:1024
	ds_read_b128 v[192:195], v110 offset:2048
	ds_read_b128 v[196:199], v110 offset:3072
	s_add_u32 s1, s36, 0x80
	s_addc_u32 s42, s37, 0
	s_and_b64 s[40:41], s[38:39], exec
	s_cselect_b32 s41, s79, s42
	s_cselect_b32 s40, s78, s1
	s_cselect_b32 s43, s83, s72
	s_cselect_b32 s42, s82, s25
	ds_read_b128 v[200:203], v165
	ds_read_b128 v[204:207], v165 offset:1024
	ds_read_b128 v[208:211], v165 offset:2048
	ds_read_b128 v[212:215], v165 offset:3072
	ds_read_b128 v[216:219], v165 offset:4096
	ds_read_b128 v[220:223], v165 offset:5120
	ds_read_b128 v[226:229], v165 offset:6144
	ds_read_b128 v[230:233], v165 offset:7168
	s_add_i32 m0, s52, 0xc000
	s_nop 0
	global_load_lds_dwordx4 v160, s[36:37]
	v_mov_b32_e32 v110, v161
	s_add_i32 m0, s52, 0xe000
	s_nop 0
	global_load_lds_dwordx4 v110, s[36:37]
	s_waitcnt vmcnt(8)
	s_waitcnt lgkmcnt(0)
	s_barrier
	s_setprio 1
	s_waitcnt lgkmcnt(0)
	v_mfma_scale_f32_16x16x128_f8f6f4 v[114:117], v[168:175], v[208:215], v[114:117], v166, v166 op_sel_hi:[0,0,0]
	v_mfma_scale_f32_16x16x128_f8f6f4 v[102:105], v[176:183], v[208:215], v[102:105], v166, v166 op_sel_hi:[0,0,0]
	v_mfma_scale_f32_16x16x128_f8f6f4 v[94:97], v[168:175], v[216:223], v[94:97], v166, v166 op_sel_hi:[0,0,0]
	v_mfma_scale_f32_16x16x128_f8f6f4 v[86:89], v[176:183], v[216:223], v[86:89], v166, v166 op_sel_hi:[0,0,0]
	v_mfma_scale_f32_16x16x128_f8f6f4 v[78:81], v[168:175], v[226:233], v[78:81], v166, v166 op_sel_hi:[0,0,0]
	v_mfma_scale_f32_16x16x128_f8f6f4 v[70:73], v[176:183], v[226:233], v[70:73], v166, v166 op_sel_hi:[0,0,0]
	v_mfma_scale_f32_16x16x128_f8f6f4 v[110:113], v[168:175], v[200:207], v[142:145], v166, v166 op_sel_hi:[0,0,0]
	v_mfma_scale_f32_16x16x128_f8f6f4 v[118:121], v[176:183], v[200:207], v[134:137], v166, v166 op_sel_hi:[0,0,0]
	s_setprio 0
	s_setprio 1
	v_mfma_scale_f32_16x16x128_f8f6f4 v[122:125], v[192:199], v[200:207], v[122:125], v166, v166 op_sel_hi:[0,0,0]
	v_mfma_scale_f32_16x16x128_f8f6f4 v[106:109], v[184:191], v[208:215], v[106:109], v166, v166 op_sel_hi:[0,0,0]
	v_mfma_scale_f32_16x16x128_f8f6f4 v[98:101], v[192:199], v[208:215], v[98:101], v166, v166 op_sel_hi:[0,0,0]
	v_mfma_scale_f32_16x16x128_f8f6f4 v[90:93], v[184:191], v[216:223], v[90:93], v166, v166 op_sel_hi:[0,0,0]
	v_mfma_scale_f32_16x16x128_f8f6f4 v[82:85], v[192:199], v[216:223], v[82:85], v166, v166 op_sel_hi:[0,0,0]
	v_mfma_scale_f32_16x16x128_f8f6f4 v[74:77], v[184:191], v[226:233], v[74:77], v166, v166 op_sel_hi:[0,0,0]
	v_mfma_scale_f32_16x16x128_f8f6f4 v[66:69], v[192:199], v[226:233], v[66:69], v166, v166 op_sel_hi:[0,0,0]
	v_mfma_scale_f32_16x16x128_f8f6f4 v[126:129], v[184:191], v[200:207], v[138:141], v166, v166 op_sel_hi:[0,0,0]
	s_setprio 0
	s_barrier
	s_add_i32 s1, s67, s45
	ds_read_b128 v[134:137], v165 offset:16384
	s_nop 1
	ds_read_b128 v[138:141], v165 offset:17408
	ds_read_b128 v[200:203], v165 offset:18432
	ds_read_b128 v[204:207], v165 offset:19456
	ds_read_b128 v[208:211], v165 offset:20480
	ds_read_b128 v[212:215], v165 offset:21504
	ds_read_b128 v[216:219], v165 offset:22528
	ds_read_b128 v[220:223], v165 offset:23552
	s_mov_b32 m0, s1
	s_nop 0
	global_load_lds_dwordx4 v158, s[42:43]
	s_add_i32 m0, s1, 0x2000
	s_add_u32 s74, s42, 0x40000
	global_load_lds_dwordx4 v159, s[42:43]
	s_addc_u32 s75, s43, 0
	s_add_i32 s1, s68, s45
	s_mov_b32 m0, s1
	s_nop 0
	global_load_lds_dwordx4 v158, s[74:75]
	s_add_i32 m0, s1, 0x2000
	s_nop 0
	global_load_lds_dwordx4 v159, s[74:75]
	s_mov_b32 m0, s52
	s_nop 0
	global_load_lds_dwordx4 v133, s[40:41]
	v_mov_b32_e32 v142, v150
	s_mov_b32 m0, s53
	s_nop 0
	global_load_lds_dwordx4 v142, s[40:41]
	s_waitcnt vmcnt(8)
	s_waitcnt lgkmcnt(0)
	s_barrier
	s_setprio 1
	s_waitcnt lgkmcnt(0)
	v_mfma_scale_f32_16x16x128_f8f6f4 v[62:65], v[168:175], v[134:141], v[62:65], v166, v166 op_sel_hi:[0,0,0]
	v_mfma_scale_f32_16x16x128_f8f6f4 v[54:57], v[176:183], v[134:141], v[54:57], v166, v166 op_sel_hi:[0,0,0]
	v_mfma_scale_f32_16x16x128_f8f6f4 v[46:49], v[168:175], v[200:207], v[46:49], v166, v166 op_sel_hi:[0,0,0]
	v_mfma_scale_f32_16x16x128_f8f6f4 v[38:41], v[176:183], v[200:207], v[38:41], v166, v166 op_sel_hi:[0,0,0]
	v_mfma_scale_f32_16x16x128_f8f6f4 v[30:33], v[168:175], v[208:215], v[30:33], v166, v166 op_sel_hi:[0,0,0]
	v_mfma_scale_f32_16x16x128_f8f6f4 v[22:25], v[176:183], v[208:215], v[22:25], v166, v166 op_sel_hi:[0,0,0]
	v_mfma_scale_f32_16x16x128_f8f6f4 v[14:17], v[168:175], v[216:223], v[14:17], v166, v166 op_sel_hi:[0,0,0]
	v_mfma_scale_f32_16x16x128_f8f6f4 v[6:9], v[176:183], v[216:223], v[6:9], v166, v166 op_sel_hi:[0,0,0]
	s_setprio 0
	s_setprio 1
	v_mfma_scale_f32_16x16x128_f8f6f4 v[58:61], v[184:191], v[134:141], v[58:61], v166, v166 op_sel_hi:[0,0,0]
	v_mfma_scale_f32_16x16x128_f8f6f4 v[50:53], v[192:199], v[134:141], v[50:53], v166, v166 op_sel_hi:[0,0,0]
	v_mfma_scale_f32_16x16x128_f8f6f4 v[42:45], v[184:191], v[200:207], v[42:45], v166, v166 op_sel_hi:[0,0,0]
	v_mfma_scale_f32_16x16x128_f8f6f4 v[34:37], v[192:199], v[200:207], v[34:37], v166, v166 op_sel_hi:[0,0,0]
	v_mfma_scale_f32_16x16x128_f8f6f4 v[26:29], v[184:191], v[208:215], v[26:29], v166, v166 op_sel_hi:[0,0,0]
	v_mfma_scale_f32_16x16x128_f8f6f4 v[18:21], v[192:199], v[208:215], v[18:21], v166, v166 op_sel_hi:[0,0,0]
	v_mfma_scale_f32_16x16x128_f8f6f4 v[10:13], v[184:191], v[216:223], v[10:13], v166, v166 op_sel_hi:[0,0,0]
	v_mfma_scale_f32_16x16x128_f8f6f4 v[2:5], v[192:199], v[216:223], v[2:5], v166, v166 op_sel_hi:[0,0,0]
	s_setprio 0
	s_barrier
; template <class Epi, bool GATHER, bool EXPERT, bool FP8>
; DI void gemm_phase(LAS unsigned char* lds, const Gemm g, const StaticOrder& S, const Epi& E) {
;     ...
;             if (GATHER && last && has_next) {
;                 o00 = sp[0] * (unsigned)(K * 2) + (unsigned)C0x2; o01 = sp[512] * (unsigned)(K * 2) + (unsigned)C1x2;
;                 o10 = sp[1024] * (unsigned)(K * 2) + (unsigned)C0x2; o11 = sp[1536] * (unsigned)(K * 2) + (unsigned)C1x2; }
;             PG8_TRIP(a1, a2, b2, a3, b3, o00, o01, o10, o11);
;             if (last) { coffA[0][0] = o00; coffA[0][1] = o01; coffA[1][0] = o10; coffA[1][1] = o11; }
;         }
	s_add_i32 s1, 0, 0x18000
	v_add_u32_e32 v134, s1, v164
	s_add_i32 s73, 0, 0x1c000
	ds_read_b128 v[168:171], v134
	ds_read_b128 v[172:175], v134 offset:1024
	ds_read_b128 v[176:179], v134 offset:2048
	ds_read_b128 v[180:183], v134 offset:3072
	v_add_u32_e32 v134, s73, v164
	ds_read_b128 v[184:187], v134
	ds_read_b128 v[188:191], v134 offset:1024
	ds_read_b128 v[192:195], v134 offset:2048
	ds_read_b128 v[196:199], v134 offset:3072
	s_mov_b32 m0, s54
	ds_read_b128 v[200:203], v165 offset:32768
	ds_read_b128 v[204:207], v165 offset:33792
	ds_read_b128 v[208:211], v165 offset:34816
	ds_read_b128 v[212:215], v165 offset:35840
	ds_read_b128 v[216:219], v165 offset:36864
	ds_read_b128 v[220:223], v165 offset:37888
	ds_read_b128 v[226:229], v165 offset:38912
	ds_read_b128 v[230:233], v165 offset:39936
	s_nop 0
	global_load_lds_dwordx4 v151, s[40:41]
	v_mov_b32_e32 v134, v152
	s_mov_b32 m0, s55
	s_nop 0
	global_load_lds_dwordx4 v134, s[40:41]
	s_waitcnt vmcnt(8)
	s_waitcnt lgkmcnt(0)
	s_barrier
	s_setprio 1
	s_waitcnt lgkmcnt(0)
	v_mfma_scale_f32_16x16x128_f8f6f4 v[142:145], v[168:175], v[200:207], v[110:113], v166, v166 op_sel_hi:[0,0,0]
	v_mfma_scale_f32_16x16x128_f8f6f4 v[134:137], v[176:183], v[200:207], v[118:121], v166, v166 op_sel_hi:[0,0,0]
	v_mfma_scale_f32_16x16x128_f8f6f4 v[114:117], v[168:175], v[208:215], v[114:117], v166, v166 op_sel_hi:[0,0,0]
	v_mfma_scale_f32_16x16x128_f8f6f4 v[102:105], v[176:183], v[208:215], v[102:105], v166, v166 op_sel_hi:[0,0,0]
	v_mfma_scale_f32_16x16x128_f8f6f4 v[94:97], v[168:175], v[216:223], v[94:97], v166, v166 op_sel_hi:[0,0,0]
	v_mfma_scale_f32_16x16x128_f8f6f4 v[86:89], v[176:183], v[216:223], v[86:89], v166, v166 op_sel_hi:[0,0,0]
	v_mfma_scale_f32_16x16x128_f8f6f4 v[78:81], v[168:175], v[226:233], v[78:81], v166, v166 op_sel_hi:[0,0,0]
	v_mfma_scale_f32_16x16x128_f8f6f4 v[70:73], v[176:183], v[226:233], v[70:73], v166, v166 op_sel_hi:[0,0,0]
	s_setprio 0
	s_setprio 1
	v_mfma_scale_f32_16x16x128_f8f6f4 v[138:141], v[184:191], v[200:207], v[126:129], v166, v166 op_sel_hi:[0,0,0]
	v_mfma_scale_f32_16x16x128_f8f6f4 v[122:125], v[192:199], v[200:207], v[122:125], v166, v166 op_sel_hi:[0,0,0]
	v_mfma_scale_f32_16x16x128_f8f6f4 v[106:109], v[184:191], v[208:215], v[106:109], v166, v166 op_sel_hi:[0,0,0]
	v_mfma_scale_f32_16x16x128_f8f6f4 v[98:101], v[192:199], v[208:215], v[98:101], v166, v166 op_sel_hi:[0,0,0]
	v_mfma_scale_f32_16x16x128_f8f6f4 v[90:93], v[184:191], v[216:223], v[90:93], v166, v166 op_sel_hi:[0,0,0]
	v_mfma_scale_f32_16x16x128_f8f6f4 v[82:85], v[192:199], v[216:223], v[82:85], v166, v166 op_sel_hi:[0,0,0]
	v_mfma_scale_f32_16x16x128_f8f6f4 v[74:77], v[184:191], v[226:233], v[74:77], v166, v166 op_sel_hi:[0,0,0]
	v_mfma_scale_f32_16x16x128_f8f6f4 v[66:69], v[192:199], v[226:233], v[66:69], v166, v166 op_sel_hi:[0,0,0]
	s_setprio 0
	s_barrier
	v_mov_b32_e32 v146, v158
	ds_read_b128 v[200:203], v165 offset:49152
	ds_read_b128 v[204:207], v165 offset:50176
	ds_read_b128 v[208:211], v165 offset:51200
	ds_read_b128 v[212:215], v165 offset:52224
	ds_read_b128 v[216:219], v165 offset:53248
	ds_read_b128 v[220:223], v165 offset:54272
	ds_read_b128 v[226:229], v165 offset:55296
	ds_read_b128 v[230:233], v165 offset:56320
	s_add_i32 s1, s1, s45
	v_lshl_add_u64 v[110:111], s[42:43], 0, v[146:147]
	v_lshl_add_u64 v[110:111], v[110:111], 0, s[88:89]
	s_mov_b32 m0, s1
	v_mov_b32_e32 v146, v159
	global_load_lds_dwordx4 v[110:111], off
	s_add_i32 m0, s1, 0x2000
	v_lshl_add_u64 v[110:111], s[42:43], 0, v[146:147]
	v_lshl_add_u64 v[110:111], v[110:111], 0, s[88:89]
	s_add_u32 s42, s42, 0x40080
	global_load_lds_dwordx4 v[110:111], off
	s_addc_u32 s43, s43, 0
	s_add_i32 s1, s73, s45
	s_mov_b32 m0, s1
	v_mov_b32_e32 v146, v133
	global_load_lds_dwordx4 v158, s[42:43]
	v_mov_b32_e32 v110, v159
	s_add_i32 m0, s1, 0x2000
	s_nop 0
	global_load_lds_dwordx4 v110, s[42:43]
	s_mov_b32 m0, s59
	v_lshl_add_u64 v[110:111], s[40:41], 0, v[146:147]
	v_lshl_add_u64 v[110:111], v[110:111], 0, s[88:89]
	v_mov_b32_e32 v146, v150
	global_load_lds_dwordx4 v[110:111], off
	s_mov_b32 m0, s60
	v_lshl_add_u64 v[110:111], s[40:41], 0, v[146:147]
	v_lshl_add_u64 v[110:111], v[110:111], 0, s[88:89]
	global_load_lds_dwordx4 v[110:111], off
	s_waitcnt vmcnt(8)
	s_waitcnt lgkmcnt(0)
	s_barrier
	s_setprio 1
	s_waitcnt lgkmcnt(0)
	v_mfma_scale_f32_16x16x128_f8f6f4 v[62:65], v[168:175], v[200:207], v[62:65], v166, v166 op_sel_hi:[0,0,0]
	v_mfma_scale_f32_16x16x128_f8f6f4 v[54:57], v[176:183], v[200:207], v[54:57], v166, v166 op_sel_hi:[0,0,0]
	v_mfma_scale_f32_16x16x128_f8f6f4 v[46:49], v[168:175], v[208:215], v[46:49], v166, v166 op_sel_hi:[0,0,0]
	v_mfma_scale_f32_16x16x128_f8f6f4 v[38:41], v[176:183], v[208:215], v[38:41], v166, v166 op_sel_hi:[0,0,0]
	v_mfma_scale_f32_16x16x128_f8f6f4 v[30:33], v[168:175], v[216:223], v[30:33], v166, v166 op_sel_hi:[0,0,0]
	v_mfma_scale_f32_16x16x128_f8f6f4 v[22:25], v[176:183], v[216:223], v[22:25], v166, v166 op_sel_hi:[0,0,0]
	v_mfma_scale_f32_16x16x128_f8f6f4 v[14:17], v[168:175], v[226:233], v[14:17], v166, v166 op_sel_hi:[0,0,0]
	v_mfma_scale_f32_16x16x128_f8f6f4 v[6:9], v[176:183], v[226:233], v[6:9], v166, v166 op_sel_hi:[0,0,0]
	s_setprio 0
	s_setprio 1
	v_mfma_scale_f32_16x16x128_f8f6f4 v[58:61], v[184:191], v[200:207], v[58:61], v166, v166 op_sel_hi:[0,0,0]
	v_mfma_scale_f32_16x16x128_f8f6f4 v[50:53], v[192:199], v[200:207], v[50:53], v166, v166 op_sel_hi:[0,0,0]
	v_mfma_scale_f32_16x16x128_f8f6f4 v[42:45], v[184:191], v[208:215], v[42:45], v166, v166 op_sel_hi:[0,0,0]
	v_mfma_scale_f32_16x16x128_f8f6f4 v[34:37], v[192:199], v[208:215], v[34:37], v166, v166 op_sel_hi:[0,0,0]
	v_mfma_scale_f32_16x16x128_f8f6f4 v[26:29], v[184:191], v[216:223], v[26:29], v166, v166 op_sel_hi:[0,0,0]
	v_mfma_scale_f32_16x16x128_f8f6f4 v[18:21], v[192:199], v[216:223], v[18:21], v166, v166 op_sel_hi:[0,0,0]
	v_mfma_scale_f32_16x16x128_f8f6f4 v[10:13], v[184:191], v[226:233], v[10:13], v166, v166 op_sel_hi:[0,0,0]
	v_mfma_scale_f32_16x16x128_f8f6f4 v[2:5], v[192:199], v[226:233], v[2:5], v166, v166 op_sel_hi:[0,0,0]
	s_add_i32 s0, s0, 2
	s_add_u32 s25, s25, 0x100
	s_addc_u32 s72, s72, 0
	s_add_u32 s36, s36, 0x100
	s_addc_u32 s37, s37, 0
	s_setprio 0
	s_barrier
	s_andn2_b64 vcc, exec, s[38:39]
	s_cbranch_vccnz .LBB0_1084
	v_mov_b32_e32 v161, v152
	v_mov_b32_e32 v160, v151
	v_mov_b32_e32 v163, v150
	v_mov_b32_e32 v162, v133
	s_branch .LBB0_1084

.LBB0_1161:
	ds_read_b128 v[128:131], v157
	ds_read_b128 v[132:135], v157 offset:1024
	ds_read_b128 v[136:139], v157 offset:2048
	ds_read_b128 v[140:143], v157 offset:3072
	ds_read_b128 v[162:165], v158
	ds_read_b128 v[166:169], v158 offset:1024
	ds_read_b128 v[170:173], v158 offset:2048
	ds_read_b128 v[174:177], v158 offset:3072
	s_add_u32 s23, s34, 0x80
	s_addc_u32 s33, s35, 0
	s_cmp_eq_u32 s21, 12
	s_cselect_b32 s37, s25, s33
	s_cselect_b32 s36, s24, s23
	s_cselect_b32 s39, s5, s1
	s_cselect_b32 s38, s4, s0
	ds_read_b128 v[178:181], v159
	ds_read_b128 v[182:185], v159 offset:1024
	ds_read_b128 v[186:189], v159 offset:2048
	ds_read_b128 v[190:193], v159 offset:3072
	ds_read_b128 v[194:197], v159 offset:4096
	ds_read_b128 v[198:201], v159 offset:5120
	ds_read_b128 v[202:205], v159 offset:6144
	ds_read_b128 v[206:209], v159 offset:7168
	s_add_i32 m0, s31, 0xc000
	s_nop 0
	global_load_lds_dwordx4 v153, s[34:35]
	s_add_i32 m0, s31, 0xe000
	s_nop 0
	global_load_lds_dwordx4 v155, s[34:35]
	s_waitcnt vmcnt(8)
	s_waitcnt lgkmcnt(0)
	s_barrier
	s_setprio 1
	s_waitcnt lgkmcnt(0)
	v_mfma_scale_f32_16x16x128_f8f6f4 v[124:127], v[128:135], v[178:185], v[124:127], v160, v160 op_sel_hi:[0,0,0]
	v_mfma_scale_f32_16x16x128_f8f6f4 v[120:123], v[136:143], v[178:185], v[120:123], v160, v160 op_sel_hi:[0,0,0]
	v_mfma_scale_f32_16x16x128_f8f6f4 v[116:119], v[128:135], v[186:193], v[116:119], v160, v160 op_sel_hi:[0,0,0]
	v_mfma_scale_f32_16x16x128_f8f6f4 v[112:115], v[136:143], v[186:193], v[112:115], v160, v160 op_sel_hi:[0,0,0]
	v_mfma_scale_f32_16x16x128_f8f6f4 v[210:213], v[128:135], v[194:201], v[92:95], v160, v160 op_sel_hi:[0,0,0]
	v_mfma_scale_f32_16x16x128_f8f6f4 v[214:217], v[136:143], v[194:201], v[88:91], v160, v160 op_sel_hi:[0,0,0]
	v_mfma_scale_f32_16x16x128_f8f6f4 v[218:221], v[128:135], v[202:209], v[84:87], v160, v160 op_sel_hi:[0,0,0]
	v_mfma_scale_f32_16x16x128_f8f6f4 v[226:229], v[136:143], v[202:209], v[80:83], v160, v160 op_sel_hi:[0,0,0]
	s_setprio 0
	s_setprio 1
	v_mfma_scale_f32_16x16x128_f8f6f4 v[108:111], v[162:169], v[178:185], v[108:111], v160, v160 op_sel_hi:[0,0,0]
	v_mfma_scale_f32_16x16x128_f8f6f4 v[104:107], v[170:177], v[178:185], v[104:107], v160, v160 op_sel_hi:[0,0,0]
	v_mfma_scale_f32_16x16x128_f8f6f4 v[100:103], v[162:169], v[186:193], v[100:103], v160, v160 op_sel_hi:[0,0,0]
	v_mfma_scale_f32_16x16x128_f8f6f4 v[96:99], v[170:177], v[186:193], v[96:99], v160, v160 op_sel_hi:[0,0,0]
	v_mfma_scale_f32_16x16x128_f8f6f4 v[230:233], v[162:169], v[194:201], v[76:79], v160, v160 op_sel_hi:[0,0,0]
	v_mfma_scale_f32_16x16x128_f8f6f4 v[194:197], v[170:177], v[194:201], v[72:75], v160, v160 op_sel_hi:[0,0,0]
	v_mfma_scale_f32_16x16x128_f8f6f4 v[198:201], v[162:169], v[202:209], v[68:71], v160, v160 op_sel_hi:[0,0,0]
	v_mfma_scale_f32_16x16x128_f8f6f4 v[202:205], v[170:177], v[202:209], v[64:67], v160, v160 op_sel_hi:[0,0,0]
	s_setprio 0
	s_barrier
	s_add_i32 s23, s57, s43
	s_nop 2
	ds_read_b128 v[64:67], v159 offset:16384
	ds_read_b128 v[68:71], v159 offset:17408
	ds_read_b128 v[72:75], v159 offset:18432
	ds_read_b128 v[76:79], v159 offset:19456
	ds_read_b128 v[80:83], v159 offset:20480
	ds_read_b128 v[84:87], v159 offset:21504
	ds_read_b128 v[88:91], v159 offset:22528
	ds_read_b128 v[92:95], v159 offset:23552
	s_mov_b32 m0, s23
	s_nop 0
	global_load_lds_dwordx4 v150, s[38:39]
	s_add_i32 m0, s23, 0x2000
	s_add_u32 s62, s38, 0x40000
	global_load_lds_dwordx4 v151, s[38:39]
	s_addc_u32 s63, s39, 0
	s_add_i32 s23, s58, s43
	s_mov_b32 m0, s23
	s_nop 0
	global_load_lds_dwordx4 v150, s[62:63]
	s_add_i32 m0, s23, 0x2000
	s_nop 0
	global_load_lds_dwordx4 v151, s[62:63]
	s_mov_b32 m0, s31
	s_nop 0
	global_load_lds_dwordx4 v152, s[36:37]
	s_mov_b32 m0, s49
	s_nop 0
	global_load_lds_dwordx4 v154, s[36:37]
	s_waitcnt vmcnt(8)
	s_waitcnt lgkmcnt(0)
	s_barrier
	s_setprio 1
	s_waitcnt lgkmcnt(0)
	v_mfma_scale_f32_16x16x128_f8f6f4 v[60:63], v[128:135], v[64:71], v[60:63], v160, v160 op_sel_hi:[0,0,0]
	v_mfma_scale_f32_16x16x128_f8f6f4 v[56:59], v[136:143], v[64:71], v[56:59], v160, v160 op_sel_hi:[0,0,0]
	v_mfma_scale_f32_16x16x128_f8f6f4 v[52:55], v[128:135], v[72:79], v[52:55], v160, v160 op_sel_hi:[0,0,0]
	v_mfma_scale_f32_16x16x128_f8f6f4 v[48:51], v[136:143], v[72:79], v[48:51], v160, v160 op_sel_hi:[0,0,0]
	v_mfma_scale_f32_16x16x128_f8f6f4 v[28:31], v[128:135], v[80:87], v[28:31], v160, v160 op_sel_hi:[0,0,0]
	v_mfma_scale_f32_16x16x128_f8f6f4 v[24:27], v[136:143], v[80:87], v[24:27], v160, v160 op_sel_hi:[0,0,0]
	v_mfma_scale_f32_16x16x128_f8f6f4 v[20:23], v[128:135], v[88:95], v[20:23], v160, v160 op_sel_hi:[0,0,0]
	v_mfma_scale_f32_16x16x128_f8f6f4 v[16:19], v[136:143], v[88:95], v[16:19], v160, v160 op_sel_hi:[0,0,0]
	s_setprio 0
	s_setprio 1
	v_mfma_scale_f32_16x16x128_f8f6f4 v[44:47], v[162:169], v[64:71], v[44:47], v160, v160 op_sel_hi:[0,0,0]
	v_mfma_scale_f32_16x16x128_f8f6f4 v[40:43], v[170:177], v[64:71], v[40:43], v160, v160 op_sel_hi:[0,0,0]
	v_mfma_scale_f32_16x16x128_f8f6f4 v[36:39], v[162:169], v[72:79], v[36:39], v160, v160 op_sel_hi:[0,0,0]
	v_mfma_scale_f32_16x16x128_f8f6f4 v[32:35], v[170:177], v[72:79], v[32:35], v160, v160 op_sel_hi:[0,0,0]
	v_mfma_scale_f32_16x16x128_f8f6f4 v[12:15], v[162:169], v[80:87], v[12:15], v160, v160 op_sel_hi:[0,0,0]
	v_mfma_scale_f32_16x16x128_f8f6f4 v[8:11], v[170:177], v[80:87], v[8:11], v160, v160 op_sel_hi:[0,0,0]
	v_mfma_scale_f32_16x16x128_f8f6f4 v[4:7], v[162:169], v[88:95], v[4:7], v160, v160 op_sel_hi:[0,0,0]
	v_mfma_scale_f32_16x16x128_f8f6f4 v[0:3], v[170:177], v[88:95], v[0:3], v160, v160 op_sel_hi:[0,0,0]
	s_setprio 0
	s_barrier
; template <class Epi, bool GATHER, bool EXPERT, bool FP8>
; DI void gemm_phase(LAS unsigned char* lds, const Gemm g, const StaticOrder& S, const Epi& E) {
;     ...
;         for (int t = 0; t < nt; t += 2) {
;             const bool last = (t == nt - 2);
;             const char* a1 = cA + (size_t)(t + 1) * kstep;
;             const char* a2 = last ? nA : cA + (size_t)(t + 2) * kstep; const char* b2 = last ? nB : cB + (size_t)(t + 2) * kstep;
;             const char* a3 = a2 + kstep; const char* b3 = b2 + kstep;
;             unsigned o00 = coffA[0][0], o01 = coffA[0][1], o10 = coffA[1][0], o11 = coffA[1][1];
;             if (GATHER && last && has_next) {
;                 o00 = sp[0] * (unsigned)(K * 2) + (unsigned)C0x2; o01 = sp[512] * (unsigned)(K * 2) + (unsigned)C1x2;
;                 o10 = sp[1024] * (unsigned)(K * 2) + (unsigned)C0x2; o11 = sp[1536] * (unsigned)(K * 2) + (unsigned)C1x2; }
;             PG8_TRIP(a1, a2, b2, a3, b3, o00, o01, o10, o11);
;             if (last) { coffA[0][0] = o00; coffA[0][1] = o01; coffA[1][0] = o10; coffA[1][1] = o11; }
;         }
	s_add_i32 s23, 0, 0x18000
	v_add_u32_e32 v64, s23, v156
	s_add_i32 s33, 0, 0x1c000
	ds_read_b128 v[128:131], v64
	ds_read_b128 v[132:135], v64 offset:1024
	ds_read_b128 v[136:139], v64 offset:2048
	ds_read_b128 v[140:143], v64 offset:3072
	v_add_u32_e32 v64, s33, v156
	ds_read_b128 v[162:165], v64
	ds_read_b128 v[166:169], v64 offset:1024
	ds_read_b128 v[170:173], v64 offset:2048
	ds_read_b128 v[174:177], v64 offset:3072
	s_mov_b32 m0, s50
	ds_read_b128 v[64:67], v159 offset:32768
	ds_read_b128 v[68:71], v159 offset:33792
	ds_read_b128 v[72:75], v159 offset:34816
	ds_read_b128 v[76:79], v159 offset:35840
	ds_read_b128 v[178:181], v159 offset:36864
	ds_read_b128 v[182:185], v159 offset:37888
	ds_read_b128 v[186:189], v159 offset:38912
	ds_read_b128 v[190:193], v159 offset:39936
	s_nop 0
	global_load_lds_dwordx4 v153, s[36:37]
	v_mov_b32_e32 v80, v155
	s_mov_b32 m0, s51
	s_nop 0
	global_load_lds_dwordx4 v80, s[36:37]
	s_waitcnt vmcnt(8)
	s_waitcnt lgkmcnt(0)
	s_barrier
	s_setprio 1
	s_waitcnt lgkmcnt(0)
	v_mfma_scale_f32_16x16x128_f8f6f4 v[124:127], v[128:135], v[64:71], v[124:127], v160, v160 op_sel_hi:[0,0,0]
	v_mfma_scale_f32_16x16x128_f8f6f4 v[120:123], v[136:143], v[64:71], v[120:123], v160, v160 op_sel_hi:[0,0,0]
	v_mfma_scale_f32_16x16x128_f8f6f4 v[116:119], v[128:135], v[72:79], v[116:119], v160, v160 op_sel_hi:[0,0,0]
	v_mfma_scale_f32_16x16x128_f8f6f4 v[112:115], v[136:143], v[72:79], v[112:115], v160, v160 op_sel_hi:[0,0,0]
	v_mfma_scale_f32_16x16x128_f8f6f4 v[92:95], v[128:135], v[178:185], v[210:213], v160, v160 op_sel_hi:[0,0,0]
	v_mfma_scale_f32_16x16x128_f8f6f4 v[88:91], v[136:143], v[178:185], v[214:217], v160, v160 op_sel_hi:[0,0,0]
	v_mfma_scale_f32_16x16x128_f8f6f4 v[84:87], v[128:135], v[186:193], v[218:221], v160, v160 op_sel_hi:[0,0,0]
	v_mfma_scale_f32_16x16x128_f8f6f4 v[80:83], v[136:143], v[186:193], v[226:229], v160, v160 op_sel_hi:[0,0,0]
	s_setprio 0
	s_setprio 1
	v_mfma_scale_f32_16x16x128_f8f6f4 v[108:111], v[162:169], v[64:71], v[108:111], v160, v160 op_sel_hi:[0,0,0]
	v_mfma_scale_f32_16x16x128_f8f6f4 v[104:107], v[170:177], v[64:71], v[104:107], v160, v160 op_sel_hi:[0,0,0]
	v_mfma_scale_f32_16x16x128_f8f6f4 v[100:103], v[162:169], v[72:79], v[100:103], v160, v160 op_sel_hi:[0,0,0]
	v_mfma_scale_f32_16x16x128_f8f6f4 v[96:99], v[170:177], v[72:79], v[96:99], v160, v160 op_sel_hi:[0,0,0]
	v_mfma_scale_f32_16x16x128_f8f6f4 v[76:79], v[162:169], v[178:185], v[230:233], v160, v160 op_sel_hi:[0,0,0]
	v_mfma_scale_f32_16x16x128_f8f6f4 v[72:75], v[170:177], v[178:185], v[194:197], v160, v160 op_sel_hi:[0,0,0]
	v_mfma_scale_f32_16x16x128_f8f6f4 v[68:71], v[162:169], v[186:193], v[198:201], v160, v160 op_sel_hi:[0,0,0]
	v_mfma_scale_f32_16x16x128_f8f6f4 v[64:67], v[170:177], v[186:193], v[202:205], v160, v160 op_sel_hi:[0,0,0]
	s_setprio 0
	s_barrier
	v_mov_b32_e32 v144, v150
	ds_read_b128 v[178:181], v159 offset:49152
	ds_read_b128 v[182:185], v159 offset:50176
	ds_read_b128 v[186:189], v159 offset:51200
	ds_read_b128 v[190:193], v159 offset:52224
	ds_read_b128 v[194:197], v159 offset:53248
	ds_read_b128 v[198:201], v159 offset:54272
	ds_read_b128 v[202:205], v159 offset:55296
	ds_read_b128 v[206:209], v159 offset:56320
	s_add_i32 s23, s23, s43
	v_lshl_add_u64 v[148:149], s[38:39], 0, v[144:145]
	v_lshl_add_u64 v[148:149], v[148:149], 0, s[14:15]
	s_mov_b32 m0, s23
	v_mov_b32_e32 v144, v151
	global_load_lds_dwordx4 v[148:149], off
	s_add_i32 m0, s23, 0x2000
	s_nop 0
	v_lshl_add_u64 v[148:149], s[38:39], 0, v[144:145]
	s_add_u32 s38, s38, 0x40080
	v_lshl_add_u64 v[148:149], v[148:149], 0, s[14:15]
	s_addc_u32 s39, s39, 0
	s_add_i32 s23, s33, s43
	global_load_lds_dwordx4 v[148:149], off
	s_mov_b32 m0, s23
	s_nop 0
	global_load_lds_dwordx4 v150, s[38:39]
	s_add_i32 m0, s23, 0x2000
	s_nop 0
	global_load_lds_dwordx4 v151, s[38:39]
	v_mov_b32_e32 v144, v152
	s_mov_b32 m0, s52
	v_lshl_add_u64 v[148:149], s[36:37], 0, v[144:145]
	v_lshl_add_u64 v[148:149], v[148:149], 0, s[14:15]
	v_mov_b32_e32 v144, v154
	global_load_lds_dwordx4 v[148:149], off
	s_mov_b32 m0, s53
	v_lshl_add_u64 v[148:149], s[36:37], 0, v[144:145]
	v_lshl_add_u64 v[148:149], v[148:149], 0, s[14:15]
	global_load_lds_dwordx4 v[148:149], off
	s_waitcnt vmcnt(8)
	s_waitcnt lgkmcnt(0)
	s_barrier
	s_setprio 1
	s_waitcnt lgkmcnt(0)
	v_mfma_scale_f32_16x16x128_f8f6f4 v[60:63], v[128:135], v[178:185], v[60:63], v160, v160 op_sel_hi:[0,0,0]
	v_mfma_scale_f32_16x16x128_f8f6f4 v[56:59], v[136:143], v[178:185], v[56:59], v160, v160 op_sel_hi:[0,0,0]
	v_mfma_scale_f32_16x16x128_f8f6f4 v[52:55], v[128:135], v[186:193], v[52:55], v160, v160 op_sel_hi:[0,0,0]
	v_mfma_scale_f32_16x16x128_f8f6f4 v[48:51], v[136:143], v[186:193], v[48:51], v160, v160 op_sel_hi:[0,0,0]
	v_mfma_scale_f32_16x16x128_f8f6f4 v[28:31], v[128:135], v[194:201], v[28:31], v160, v160 op_sel_hi:[0,0,0]
	v_mfma_scale_f32_16x16x128_f8f6f4 v[24:27], v[136:143], v[194:201], v[24:27], v160, v160 op_sel_hi:[0,0,0]
	v_mfma_scale_f32_16x16x128_f8f6f4 v[20:23], v[128:135], v[202:209], v[20:23], v160, v160 op_sel_hi:[0,0,0]
	v_mfma_scale_f32_16x16x128_f8f6f4 v[16:19], v[136:143], v[202:209], v[16:19], v160, v160 op_sel_hi:[0,0,0]
	s_setprio 0
	s_setprio 1
	v_mfma_scale_f32_16x16x128_f8f6f4 v[44:47], v[162:169], v[178:185], v[44:47], v160, v160 op_sel_hi:[0,0,0]
	v_mfma_scale_f32_16x16x128_f8f6f4 v[40:43], v[170:177], v[178:185], v[40:43], v160, v160 op_sel_hi:[0,0,0]
	v_mfma_scale_f32_16x16x128_f8f6f4 v[36:39], v[162:169], v[186:193], v[36:39], v160, v160 op_sel_hi:[0,0,0]
	v_mfma_scale_f32_16x16x128_f8f6f4 v[32:35], v[170:177], v[186:193], v[32:35], v160, v160 op_sel_hi:[0,0,0]
	v_mfma_scale_f32_16x16x128_f8f6f4 v[12:15], v[162:169], v[194:201], v[12:15], v160, v160 op_sel_hi:[0,0,0]
	v_mfma_scale_f32_16x16x128_f8f6f4 v[8:11], v[170:177], v[194:201], v[8:11], v160, v160 op_sel_hi:[0,0,0]
	v_mfma_scale_f32_16x16x128_f8f6f4 v[4:7], v[162:169], v[202:209], v[4:7], v160, v160 op_sel_hi:[0,0,0]
	v_mfma_scale_f32_16x16x128_f8f6f4 v[0:3], v[170:177], v[202:209], v[0:3], v160, v160 op_sel_hi:[0,0,0]
	s_add_i32 s21, s21, 2
	s_add_u32 s0, s0, 0x100
	s_addc_u32 s1, s1, 0
	s_add_u32 s34, s34, 0x100
	s_addc_u32 s35, s35, 0
	s_cmp_gt_u32 s21, 13
	s_setprio 0
	s_barrier
	s_cbranch_scc0 .LBB0_1161
	s_and_b64 vcc, exec, s[16:17]
	s_cbranch_vccz .LBB0_1164
	s_barrier
